# baseline (speedup 1.0000x reference)
.LBB2_9:
	s_waitcnt lgkmcnt(12)
	v_mfma_f32_32x32x16_f16 v[16:31], v[140:143], v[172:175], v[16:31]
	v_exp_f32_e32 v99, v99
	v_exp_f32_e32 v100, v100
	v_exp_f32_e32 v101, v101
	v_add_u32_e32 v60, s29, v190
	ds_read_b128 v[56:59], v60
	ds_read_b128 v[176:179], v60 offset:512
	s_waitcnt lgkmcnt(12)
	v_mfma_f32_32x32x16_f16 v[0:15], v[136:139], v[64:67], v[0:15]
	v_exp_f32_e32 v102, v102
	v_exp_f32_e32 v103, v103
	v_exp_f32_e32 v104, v104
	ds_read_b128 v[172:175], v60 offset:2048
	ds_read_b128 v[168:171], v60 offset:2560
	s_waitcnt lgkmcnt(12)
	v_mfma_f32_32x32x16_f16 v[16:31], v[136:139], v[68:71], v[16:31]
	v_exp_f32_e32 v105, v105
	v_exp_f32_e32 v106, v106
	v_exp_f32_e32 v107, v107
	ds_read_b128 v[164:167], v60 offset:4096
	ds_read_b128 v[160:163], v60 offset:4608
	s_waitcnt lgkmcnt(12)
	v_mfma_f32_32x32x16_f16 v[0:15], v[132:135], v[76:79], v[0:15]
	v_exp_f32_e32 v108, v108
	v_exp_f32_e32 v109, v109
	v_exp_f32_e32 v110, v110
	ds_read_b128 v[156:159], v60 offset:6144
	ds_read_b128 v[152:155], v60 offset:6656
	s_waitcnt lgkmcnt(12)
	v_mfma_f32_32x32x16_f16 v[16:31], v[132:135], v[48:51], v[16:31]
	v_exp_f32_e32 v111, v111
	v_exp_f32_e32 v80, v80
	v_exp_f32_e32 v81, v81
	s_waitcnt lgkmcnt(10)
	v_mfma_f32_32x32x16_f16 v[0:15], v[128:131], v[72:75], v[0:15]
	v_exp_f32_e32 v82, v82
	v_exp_f32_e32 v83, v83
	v_exp_f32_e32 v84, v84
	s_waitcnt lgkmcnt(8)
	v_mfma_f32_32x32x16_f16 v[16:31], v[128:131], v[52:55], v[16:31]
	s_waitcnt vmcnt(2) lgkmcnt(0)
	s_barrier
	v_exp_f32_e32 v85, v85
	v_exp_f32_e32 v86, v86
	v_exp_f32_e32 v87, v87
	s_andn2_b64 vcc, exec, s[8:9]
	s_cbranch_vccnz .LBB2_11
	v_add_u32_e32 v64, s23, v184
	ds_read_b128 v[48:51], v64 offset:49248
	ds_read_b128 v[52:55], v64 offset:49216
	ds_read_b128 v[60:63], v64 offset:49184
	ds_read_b128 v[64:67], v64 offset:49152
	s_waitcnt lgkmcnt(3)
	v_pk_mul_f32 v[12:13], v[12:13], v[48:49]
	s_waitcnt lgkmcnt(2)
	v_pk_mul_f32 v[8:9], v[8:9], v[52:53]
	s_waitcnt lgkmcnt(1)
	v_pk_mul_f32 v[4:5], v[4:5], v[60:61]
	v_pk_mul_f32 v[14:15], v[14:15], v[50:51]
	v_pk_mul_f32 v[10:11], v[10:11], v[54:55]
	v_pk_mul_f32 v[6:7], v[6:7], v[62:63]
	s_waitcnt lgkmcnt(0)
	v_pk_mul_f32 v[2:3], v[2:3], v[66:67]
	v_pk_mul_f32 v[0:1], v[0:1], v[64:65]
	v_pk_mul_f32 v[28:29], v[28:29], v[48:49]
	v_pk_mul_f32 v[24:25], v[24:25], v[52:53]
	v_pk_mul_f32 v[20:21], v[20:21], v[60:61]
	v_pk_mul_f32 v[30:31], v[30:31], v[50:51]
	v_pk_mul_f32 v[26:27], v[26:27], v[54:55]
	v_pk_mul_f32 v[22:23], v[22:23], v[62:63]
	v_pk_mul_f32 v[18:19], v[18:19], v[66:67]
	v_pk_mul_f32 v[16:17], v[16:17], v[64:65]

.LBB2_15:
	s_waitcnt lgkmcnt(12)
	v_mfma_f32_32x32x16_f16 v[16:31], v[140:143], v[144:147], v[16:31]
	v_exp_f32_e32 v67, v67
	v_exp_f32_e32 v68, v68
	v_exp_f32_e32 v69, v69
	v_add_u32_e32 v88, s33, v190
	ds_read_b128 v[172:175], v88
	ds_read_b128 v[168:171], v88 offset:512
	s_waitcnt lgkmcnt(12)
	v_mfma_f32_32x32x16_f16 v[0:15], v[136:139], v[96:99], v[0:15]
	v_exp_f32_e32 v70, v70
	v_exp_f32_e32 v71, v71
	v_exp_f32_e32 v72, v72
	ds_read_b128 v[164:167], v88 offset:2048
	ds_read_b128 v[160:163], v88 offset:2560
	s_waitcnt lgkmcnt(12)
	v_mfma_f32_32x32x16_f16 v[16:31], v[136:139], v[100:103], v[16:31]
	v_exp_f32_e32 v73, v73
	v_exp_f32_e32 v74, v74
	v_exp_f32_e32 v75, v75
	ds_read_b128 v[156:159], v88 offset:4096
	ds_read_b128 v[152:155], v88 offset:4608
	s_waitcnt lgkmcnt(12)
	v_mfma_f32_32x32x16_f16 v[0:15], v[132:135], v[104:107], v[0:15]
	v_exp_f32_e32 v76, v76
	v_exp_f32_e32 v77, v77
	v_exp_f32_e32 v78, v78
	ds_read_b128 v[148:151], v88 offset:6144
	ds_read_b128 v[144:147], v88 offset:6656
	s_waitcnt lgkmcnt(12)
	v_mfma_f32_32x32x16_f16 v[16:31], v[132:135], v[80:83], v[16:31]
	v_exp_f32_e32 v79, v79
	v_exp_f32_e32 v48, v48
	v_exp_f32_e32 v49, v49
	s_waitcnt lgkmcnt(10)
	v_mfma_f32_32x32x16_f16 v[0:15], v[128:131], v[108:111], v[0:15]
	v_exp_f32_e32 v50, v50
	v_exp_f32_e32 v51, v51
	v_exp_f32_e32 v52, v52
	s_waitcnt lgkmcnt(8)
	v_mfma_f32_32x32x16_f16 v[16:31], v[128:131], v[84:87], v[16:31]
	s_waitcnt vmcnt(2) lgkmcnt(0)
	s_barrier
	v_exp_f32_e32 v53, v53
	v_exp_f32_e32 v54, v54
	v_exp_f32_e32 v55, v55
	s_andn2_b64 vcc, exec, s[8:9]
	s_cbranch_vccnz .LBB2_17
	v_add_u32_e32 v92, s23, v184
	ds_read_b128 v[80:83], v92 offset:49248
	ds_read_b128 v[84:87], v92 offset:49216
	ds_read_b128 v[88:91], v92 offset:49152
	ds_read_b128 v[92:95], v92 offset:49184
	s_waitcnt lgkmcnt(3)
	v_pk_mul_f32 v[14:15], v[14:15], v[82:83]
	v_pk_mul_f32 v[12:13], v[12:13], v[80:81]
	s_waitcnt lgkmcnt(2)
	v_pk_mul_f32 v[10:11], v[10:11], v[86:87]
	v_pk_mul_f32 v[8:9], v[8:9], v[84:85]
	s_waitcnt lgkmcnt(0)
	v_pk_mul_f32 v[6:7], v[6:7], v[94:95]
	v_pk_mul_f32 v[4:5], v[4:5], v[92:93]
	v_pk_mul_f32 v[2:3], v[2:3], v[90:91]
	v_pk_mul_f32 v[0:1], v[0:1], v[88:89]
	v_pk_mul_f32 v[30:31], v[30:31], v[82:83]
	v_pk_mul_f32 v[28:29], v[28:29], v[80:81]
	v_pk_mul_f32 v[26:27], v[26:27], v[86:87]
	v_pk_mul_f32 v[24:25], v[24:25], v[84:85]
	v_pk_mul_f32 v[22:23], v[22:23], v[94:95]
	v_pk_mul_f32 v[20:21], v[20:21], v[92:93]
	v_pk_mul_f32 v[18:19], v[18:19], v[90:91]
	v_pk_mul_f32 v[16:17], v[16:17], v[88:89]
